# layer 3 (last reader) loads the f16 edge stream with nt via a duplicated gather; layers 1-2 keep default policy
# baseline (speedup 1.0000x reference)
.LBB5_24:
	s_and_b32 s0, s26, 12
	s_cmp_eq_u32 s0, 12
	s_cbranch_scc1 .Ll1_last
	v_or_b32_e32 v46, 1, v35
	v_add_u32_e32 v46, s24, v46
	v_min_i32_e32 v46, 0x1869f, v46
	v_lshl_add_u32 v46, v46, 8, v26
	global_load_dwordx4 v[30:33], v46, s[4:5]
	s_mov_b64 s[22:23], exec
	s_movk_i32 s0, 0x2200
	v_sub_u32_e32 v27, v44, v28
	v_lshl_add_u32 v27, v27, 2, s0
	v_lshl_add_u32 v29, v44, 8, v26
	v_cmp_lt_i32_e64 s[2:3], v44, v45
	v_add_u32_e32 v46, 1, v44
	v_cmp_lt_i32_e64 s[16:17], v46, v45
	v_add_u32_e32 v46, 2, v44
	v_cmp_lt_i32_e64 s[18:19], v46, v45
	v_add_u32_e32 v46, 3, v44
	v_cmp_lt_i32_e64 s[20:21], v46, v45
	s_mov_b64 exec, s[2:3]
	ds_read_b32 v2, v27 offset:0
	global_load_dwordx4 v[4:7], v29, s[12:13] offset:0
	s_waitcnt lgkmcnt(0)
	v_lshl_add_u32 v2, v2, 8, v26
	global_load_dwordx4 v[8:11], v2, s[4:5]
	ds_read_b32 v2, v27 offset:16
	s_mov_b64 exec, s[16:17]
	ds_read_b32 v3, v27 offset:4
	global_load_dwordx4 v[12:15], v29, s[12:13] offset:256
	s_waitcnt lgkmcnt(0)
	v_lshl_add_u32 v3, v3, 8, v26
	global_load_dwordx4 v[16:19], v3, s[4:5]
	ds_read_b32 v3, v27 offset:20
	s_mov_b64 exec, s[18:19]
	ds_read_b32 v24, v27 offset:8
	global_load_dwordx4 v[20:23], v29, s[12:13] offset:512
	s_waitcnt lgkmcnt(0)
	v_lshl_add_u32 v24, v24, 8, v26
	global_load_dwordx4 v[50:53], v24, s[4:5]
	ds_read_b32 v24, v27 offset:24
	s_mov_b64 exec, s[20:21]
	ds_read_b32 v25, v27 offset:12
	global_load_dwordx4 v[54:57], v29, s[12:13] offset:768
	s_waitcnt lgkmcnt(0)
	v_lshl_add_u32 v25, v25, 8, v26
	global_load_dwordx4 v[58:61], v25, s[4:5]
	ds_read_b32 v25, v27 offset:28
	s_mov_b64 exec, s[22:23]
	s_cmp_eq_u64 s[2:3], 0
	s_cbranch_scc1 .Ll1a_p1_empty

.Ll1_last:
	v_or_b32_e32 v46, 1, v35
	v_add_u32_e32 v46, s24, v46
	v_min_i32_e32 v46, 0x1869f, v46
	v_lshl_add_u32 v46, v46, 8, v26
	global_load_dwordx4 v[30:33], v46, s[4:5]
	s_mov_b64 s[22:23], exec
	s_movk_i32 s0, 0x2200
	v_sub_u32_e32 v27, v44, v28
	v_lshl_add_u32 v27, v27, 2, s0
	v_lshl_add_u32 v29, v44, 8, v26
	v_cmp_lt_i32_e64 s[2:3], v44, v45
	v_add_u32_e32 v46, 1, v44
	v_cmp_lt_i32_e64 s[16:17], v46, v45
	v_add_u32_e32 v46, 2, v44
	v_cmp_lt_i32_e64 s[18:19], v46, v45
	v_add_u32_e32 v46, 3, v44
	v_cmp_lt_i32_e64 s[20:21], v46, v45
	s_mov_b64 exec, s[2:3]
	ds_read_b32 v2, v27 offset:0
	global_load_dwordx4 v[4:7], v29, s[12:13] offset:0 nt
	s_waitcnt lgkmcnt(0)
	v_lshl_add_u32 v2, v2, 8, v26
	global_load_dwordx4 v[8:11], v2, s[4:5]
	ds_read_b32 v2, v27 offset:16
	s_mov_b64 exec, s[16:17]
	ds_read_b32 v3, v27 offset:4
	global_load_dwordx4 v[12:15], v29, s[12:13] offset:256 nt
	s_waitcnt lgkmcnt(0)
	v_lshl_add_u32 v3, v3, 8, v26
	global_load_dwordx4 v[16:19], v3, s[4:5]
	ds_read_b32 v3, v27 offset:20
	s_mov_b64 exec, s[18:19]
	ds_read_b32 v24, v27 offset:8
	global_load_dwordx4 v[20:23], v29, s[12:13] offset:512 nt
	s_waitcnt lgkmcnt(0)
	v_lshl_add_u32 v24, v24, 8, v26
	global_load_dwordx4 v[50:53], v24, s[4:5]
	ds_read_b32 v24, v27 offset:24
	s_mov_b64 exec, s[20:21]
	ds_read_b32 v25, v27 offset:12
	global_load_dwordx4 v[54:57], v29, s[12:13] offset:768 nt
	s_waitcnt lgkmcnt(0)
	v_lshl_add_u32 v25, v25, 8, v26
	global_load_dwordx4 v[58:61], v25, s[4:5]
	ds_read_b32 v25, v27 offset:28
	s_mov_b64 exec, s[22:23]
	s_cmp_eq_u64 s[2:3], 0
	s_cbranch_scc1 .Ll1z_p1_empty
.Ll1z_p1_loop:
	s_mov_b64 exec, s[2:3]
	s_waitcnt vmcnt(6)
	v_fma_mix_f32 v46, v8, 1.0, v4 op_sel_hi:[1,0,1]
	v_fma_mix_f32 v47, v8, 1.0, v4 op_sel:[1,0,1] op_sel_hi:[1,0,1]
	v_fma_mix_f32 v48, v9, 1.0, v5 op_sel_hi:[1,0,1]
	v_fma_mix_f32 v49, v9, 1.0, v5 op_sel:[1,0,1] op_sel_hi:[1,0,1]
	v_max_f32_e32 v46, 0, v46
	v_max_f32_e32 v47, 0, v47
	v_max_f32_e32 v48, 0, v48
	v_max_f32_e32 v49, 0, v49
	v_pk_add_f32 v[42:43], v[42:43], v[46:47]
	v_pk_add_f32 v[40:41], v[40:41], v[48:49]
	v_fma_mix_f32 v46, v10, 1.0, v6 op_sel_hi:[1,0,1]
	v_fma_mix_f32 v47, v10, 1.0, v6 op_sel:[1,0,1] op_sel_hi:[1,0,1]
	v_fma_mix_f32 v48, v11, 1.0, v7 op_sel_hi:[1,0,1]
	v_fma_mix_f32 v49, v11, 1.0, v7 op_sel:[1,0,1] op_sel_hi:[1,0,1]
	v_max_f32_e32 v46, 0, v46
	v_max_f32_e32 v47, 0, v47
	v_max_f32_e32 v48, 0, v48
	v_max_f32_e32 v49, 0, v49
	v_pk_add_f32 v[38:39], v[38:39], v[46:47]
	v_pk_add_f32 v[36:37], v[36:37], v[48:49]
	v_add_u32_e32 v46, 4, v44
	v_cmp_lt_i32_e64 s[2:3], v46, v45
	s_mov_b64 exec, s[2:3]
	global_load_dwordx4 v[4:7], v29, s[12:13] offset:1024 nt
	s_waitcnt lgkmcnt(0)
	v_lshl_add_u32 v2, v2, 8, v26
	global_load_dwordx4 v[8:11], v2, s[4:5]
	ds_read_b32 v2, v27 offset:32
	s_mov_b64 exec, s[16:17]
	s_waitcnt vmcnt(6)
	v_fma_mix_f32 v46, v16, 1.0, v12 op_sel_hi:[1,0,1]
	v_fma_mix_f32 v47, v16, 1.0, v12 op_sel:[1,0,1] op_sel_hi:[1,0,1]
	v_fma_mix_f32 v48, v17, 1.0, v13 op_sel_hi:[1,0,1]
	v_fma_mix_f32 v49, v17, 1.0, v13 op_sel:[1,0,1] op_sel_hi:[1,0,1]
	v_max_f32_e32 v46, 0, v46
	v_max_f32_e32 v47, 0, v47
	v_max_f32_e32 v48, 0, v48
	v_max_f32_e32 v49, 0, v49
	v_pk_add_f32 v[42:43], v[42:43], v[46:47]
	v_pk_add_f32 v[40:41], v[40:41], v[48:49]
	v_fma_mix_f32 v46, v18, 1.0, v14 op_sel_hi:[1,0,1]
	v_fma_mix_f32 v47, v18, 1.0, v14 op_sel:[1,0,1] op_sel_hi:[1,0,1]
	v_fma_mix_f32 v48, v19, 1.0, v15 op_sel_hi:[1,0,1]
	v_fma_mix_f32 v49, v19, 1.0, v15 op_sel:[1,0,1] op_sel_hi:[1,0,1]
	v_max_f32_e32 v46, 0, v46
	v_max_f32_e32 v47, 0, v47
	v_max_f32_e32 v48, 0, v48
	v_max_f32_e32 v49, 0, v49
	v_pk_add_f32 v[38:39], v[38:39], v[46:47]
	v_pk_add_f32 v[36:37], v[36:37], v[48:49]
	v_add_u32_e32 v46, 5, v44
	v_cmp_lt_i32_e64 s[16:17], v46, v45
	s_mov_b64 exec, s[16:17]
	global_load_dwordx4 v[12:15], v29, s[12:13] offset:1280 nt
	s_waitcnt lgkmcnt(0)
	v_lshl_add_u32 v3, v3, 8, v26
	global_load_dwordx4 v[16:19], v3, s[4:5]
	ds_read_b32 v3, v27 offset:36
	s_mov_b64 exec, s[18:19]
	s_waitcnt vmcnt(6)
	v_fma_mix_f32 v46, v50, 1.0, v20 op_sel_hi:[1,0,1]
	v_fma_mix_f32 v47, v50, 1.0, v20 op_sel:[1,0,1] op_sel_hi:[1,0,1]
	v_fma_mix_f32 v48, v51, 1.0, v21 op_sel_hi:[1,0,1]
	v_fma_mix_f32 v49, v51, 1.0, v21 op_sel:[1,0,1] op_sel_hi:[1,0,1]
	v_max_f32_e32 v46, 0, v46
	v_max_f32_e32 v47, 0, v47
	v_max_f32_e32 v48, 0, v48
	v_max_f32_e32 v49, 0, v49
	v_pk_add_f32 v[42:43], v[42:43], v[46:47]
	v_pk_add_f32 v[40:41], v[40:41], v[48:49]
	v_fma_mix_f32 v46, v52, 1.0, v22 op_sel_hi:[1,0,1]
	v_fma_mix_f32 v47, v52, 1.0, v22 op_sel:[1,0,1] op_sel_hi:[1,0,1]
	v_fma_mix_f32 v48, v53, 1.0, v23 op_sel_hi:[1,0,1]
	v_fma_mix_f32 v49, v53, 1.0, v23 op_sel:[1,0,1] op_sel_hi:[1,0,1]
	v_max_f32_e32 v46, 0, v46
	v_max_f32_e32 v47, 0, v47
	v_max_f32_e32 v48, 0, v48
	v_max_f32_e32 v49, 0, v49
	v_pk_add_f32 v[38:39], v[38:39], v[46:47]
	v_pk_add_f32 v[36:37], v[36:37], v[48:49]
	v_add_u32_e32 v46, 6, v44
	v_cmp_lt_i32_e64 s[18:19], v46, v45
	s_mov_b64 exec, s[18:19]
	global_load_dwordx4 v[20:23], v29, s[12:13] offset:1536 nt
	s_waitcnt lgkmcnt(0)
	v_lshl_add_u32 v24, v24, 8, v26
	global_load_dwordx4 v[50:53], v24, s[4:5]
	ds_read_b32 v24, v27 offset:40
	s_mov_b64 exec, s[20:21]
	s_waitcnt vmcnt(6)
	v_fma_mix_f32 v46, v58, 1.0, v54 op_sel_hi:[1,0,1]
	v_fma_mix_f32 v47, v58, 1.0, v54 op_sel:[1,0,1] op_sel_hi:[1,0,1]
	v_fma_mix_f32 v48, v59, 1.0, v55 op_sel_hi:[1,0,1]
	v_fma_mix_f32 v49, v59, 1.0, v55 op_sel:[1,0,1] op_sel_hi:[1,0,1]
	v_max_f32_e32 v46, 0, v46
	v_max_f32_e32 v47, 0, v47
	v_max_f32_e32 v48, 0, v48
	v_max_f32_e32 v49, 0, v49
	v_pk_add_f32 v[42:43], v[42:43], v[46:47]
	v_pk_add_f32 v[40:41], v[40:41], v[48:49]
	v_fma_mix_f32 v46, v60, 1.0, v56 op_sel_hi:[1,0,1]
	v_fma_mix_f32 v47, v60, 1.0, v56 op_sel:[1,0,1] op_sel_hi:[1,0,1]
	v_fma_mix_f32 v48, v61, 1.0, v57 op_sel_hi:[1,0,1]
	v_fma_mix_f32 v49, v61, 1.0, v57 op_sel:[1,0,1] op_sel_hi:[1,0,1]
	v_max_f32_e32 v46, 0, v46
	v_max_f32_e32 v47, 0, v47
	v_max_f32_e32 v48, 0, v48
	v_max_f32_e32 v49, 0, v49
	v_pk_add_f32 v[38:39], v[38:39], v[46:47]
	v_pk_add_f32 v[36:37], v[36:37], v[48:49]
	v_add_u32_e32 v46, 7, v44
	v_cmp_lt_i32_e64 s[20:21], v46, v45
	s_mov_b64 exec, s[20:21]
	global_load_dwordx4 v[54:57], v29, s[12:13] offset:1792 nt
	s_waitcnt lgkmcnt(0)
	v_lshl_add_u32 v25, v25, 8, v26
	global_load_dwordx4 v[58:61], v25, s[4:5]
	ds_read_b32 v25, v27 offset:44
	s_mov_b64 exec, s[22:23]
	v_add_u32_e32 v44, 4, v44
	v_add_u32_e32 v27, 16, v27
	v_add_u32_e32 v29, 0x400, v29
	s_cmp_lg_u64 s[2:3], 0
	s_cbranch_scc1 .Ll1z_p1_loop
	s_branch .Ll1z_p1_done

.Ll1z_p1_done:
	s_movk_i32 s2, 0x110
	v_cvt_pk_f16_f32 v5, v36, v37
	v_cvt_pk_f16_f32 v4, v38, v39
	v_cvt_pk_f16_f32 v3, v40, v41
	v_cvt_pk_f16_f32 v2, v42, v43
	v_and_b32_e32 v46, 30, v35
	v_mad_u32_u24 v46, v46, s2, v26
	ds_write_b128 v46, v[2:5]
	v_or_b32_e32 v47, 1, v35
	v_mov_b32_e32 v46, 0x3200
	v_lshl_or_b32 v46, v47, 2, v46
	ds_read2_b32 v[44:45], v46 offset1:1
	v_add_u32_e32 v46, s24, v47
	s_mov_b32 s2, 0x186a0
	v_cmp_gt_i32_e32 vcc, s2, v46
	v_cvt_f32_f16_e32 v42, v30
	v_cvt_f32_f16_sdwa v43, v30 dst_sel:DWORD dst_unused:UNUSED_PAD src0_sel:WORD_1
	v_cvt_f32_f16_e32 v40, v31
	v_cvt_f32_f16_sdwa v41, v31 dst_sel:DWORD dst_unused:UNUSED_PAD src0_sel:WORD_1
	v_cvt_f32_f16_e32 v38, v32
	v_cvt_f32_f16_sdwa v39, v32 dst_sel:DWORD dst_unused:UNUSED_PAD src0_sel:WORD_1
	v_cvt_f32_f16_e32 v36, v33
	v_cvt_f32_f16_sdwa v37, v33 dst_sel:DWORD dst_unused:UNUSED_PAD src0_sel:WORD_1
	v_mul_f32_e32 v36, v34, v36
	v_mul_f32_e32 v37, v34, v37
	v_mul_f32_e32 v38, v34, v38
	v_mul_f32_e32 v39, v34, v39
	v_mul_f32_e32 v40, v34, v40
	v_mul_f32_e32 v41, v34, v41
	v_mul_f32_e32 v42, v34, v42
	v_mul_f32_e32 v43, v34, v43
	v_cndmask_b32_e32 v36, 0, v36, vcc
	v_cndmask_b32_e32 v37, 0, v37, vcc
	v_cndmask_b32_e32 v38, 0, v38, vcc
	v_cndmask_b32_e32 v39, 0, v39, vcc
	v_cndmask_b32_e32 v40, 0, v40, vcc
	v_cndmask_b32_e32 v41, 0, v41, vcc
	v_cndmask_b32_e32 v42, 0, v42, vcc
	v_cndmask_b32_e32 v43, 0, v43, vcc
	s_waitcnt lgkmcnt(0)
	v_sub_u32_e32 v27, v44, v28
	v_lshl_add_u32 v27, v27, 2, s0
	v_lshl_add_u32 v29, v44, 8, v26
	v_cmp_lt_i32_e64 s[2:3], v44, v45
	v_add_u32_e32 v46, 1, v44
	v_cmp_lt_i32_e64 s[16:17], v46, v45
	v_add_u32_e32 v46, 2, v44
	v_cmp_lt_i32_e64 s[18:19], v46, v45
	v_add_u32_e32 v46, 3, v44
	v_cmp_lt_i32_e64 s[20:21], v46, v45
	s_mov_b64 exec, s[2:3]
	ds_read_b32 v2, v27 offset:0
	global_load_dwordx4 v[4:7], v29, s[12:13] offset:0 nt
	s_waitcnt lgkmcnt(0)
	v_lshl_add_u32 v2, v2, 8, v26
	global_load_dwordx4 v[8:11], v2, s[4:5]
	ds_read_b32 v2, v27 offset:16
	s_mov_b64 exec, s[16:17]
	ds_read_b32 v3, v27 offset:4
	global_load_dwordx4 v[12:15], v29, s[12:13] offset:256 nt
	s_waitcnt lgkmcnt(0)
	v_lshl_add_u32 v3, v3, 8, v26
	global_load_dwordx4 v[16:19], v3, s[4:5]
	ds_read_b32 v3, v27 offset:20
	s_mov_b64 exec, s[18:19]
	ds_read_b32 v24, v27 offset:8
	global_load_dwordx4 v[20:23], v29, s[12:13] offset:512 nt
	s_waitcnt lgkmcnt(0)
	v_lshl_add_u32 v24, v24, 8, v26
	global_load_dwordx4 v[50:53], v24, s[4:5]
	ds_read_b32 v24, v27 offset:24
	s_mov_b64 exec, s[20:21]
	ds_read_b32 v25, v27 offset:12
	global_load_dwordx4 v[54:57], v29, s[12:13] offset:768 nt
	s_waitcnt lgkmcnt(0)
	v_lshl_add_u32 v25, v25, 8, v26
	global_load_dwordx4 v[58:61], v25, s[4:5]
	ds_read_b32 v25, v27 offset:28
	s_mov_b64 exec, s[22:23]
	s_cmp_eq_u64 s[2:3], 0
	s_cbranch_scc1 .Ll1z_p2_empty
